# speedup vs baseline: 1.0094x; 1.0039x over previous
.LBB1_235:
	v_add_u32_e32 v0, s66, v0
	v_subrev_u32_e32 v0, 0x100, v0
	s_movk_i32 s0, 0xf0
	v_cmp_gt_u32_e32 vcc, s0, v0
	s_and_saveexec_b64 s[0:1], vcc
	s_cbranch_execz .Lepi_idle
	s_load_dwordx4 s[68:71], s[14:15], 0x0
	s_load_dwordx2 s[72:73], s[14:15], 0x10
	s_movk_i32 s0, 0x77
	v_mov_b32_e32 v1, 0xffffff88
	v_cmp_lt_u32_e32 vcc, s0, v0
	v_mov_b32_e32 v2, 0x44704000
	s_mov_b32 s0, 0xf800000
	v_cndmask_b32_e32 v1, 0, v1, vcc
	v_add_u32_e32 v0, v1, v0
	v_cvt_f32_u32_e32 v1, v0
	s_mov_b32 s5, 0x17800
	s_mov_b32 s4, 0x3eb17218
	v_fmac_f32_e32 v2, 0xc1000000, v1
	v_sqrt_f32_e32 v1, v2
	s_nop 0
	v_sub_f32_e32 v1, 0x41f80000, v1
	v_mul_f32_e32 v1, 0.5, v1
	v_cvt_i32_f32_e32 v1, v1
	s_and_b64 s[0:1], exec, s[16:17]
	s_cselect_b32 s2, s40, s38
	s_cselect_b32 s3, s39, s33
	v_sub_u32_e32 v2, 31, v1
	v_mul_u32_u24_e32 v2, v2, v1
	v_lshrrev_b32_e32 v2, 1, v2
	v_cmp_gt_i32_e64 s[0:1], v2, v0
	s_nop 1
	v_subbrev_co_u32_e64 v1, s[0:1], 0, v1, s[0:1]
	v_add_u32_e32 v2, 1, v1
	v_sub_u32_e32 v3, 30, v1
	v_mul_u32_u24_e32 v3, v2, v3
	v_lshrrev_b32_e32 v4, 31, v3
	v_add_u32_e32 v3, v3, v4
	v_ashrrev_i32_e32 v3, 1, v3
	v_cmp_gt_i32_e64 s[0:1], v3, v0
	s_nop 1
	v_cndmask_b32_e64 v12, v2, v1, s[0:1]
	v_sub_u32_e32 v1, 31, v12
	v_mul_u32_u24_e32 v1, v1, v12
	v_lshrrev_b32_e32 v1, 1, v1
	v_sub_u32_e32 v0, v0, v1
	v_cndmask_b32_e64 v1, 0, 16, vcc
	v_lshl_or_b32 v1, s2, 5, v1
	v_add_u32_e32 v1, v1, v12
	v_sub_u32_e32 v2, 0xff, v1
	v_mul_u32_u24_e32 v1, v2, v1
	v_lshrrev_b32_e32 v1, 1, v1
	v_add3_u32 v13, v12, v0, 1
	v_add_u32_e32 v0, v1, v0
	v_ashrrev_i32_e32 v1, 31, v0
	v_mov_b32_e32 v2, 0x1fc0
	v_mad_u64_u32 v[0:1], s[0:1], s3, v2, v[0:1]
	v_mad_u64_u32 v[4:5], s[0:1], v0, 24, s[10:11]
	v_mad_i32_i24 v5, v1, 24, v5
	v_mov_b32_e32 v0, 0x17800
	v_lshl_add_u32 v14, v12, 2, v0
	v_mov_b32_e32 v0, 0x60
	v_cndmask_b32_e32 v15, 0, v0, vcc
	v_lshlrev_b32_e32 v16, 2, v13
	v_add_lshl_u32 v0, v15, v12, 6
	v_add3_u32 v16, v0, v16, s5
	v_add_u32_e32 v1, v15, v13
	v_lshl_add_u32 v17, v1, 6, v14
	ds_read_b32 v0, v16
	ds_read_b32 v2, v17
	ds_read_b32 v1, v16 offset:1024
	ds_read_b32 v3, v17 offset:1024
	ds_read_b32 v6, v16 offset:2048
	ds_read_b32 v8, v17 offset:2048
	ds_read_b32 v7, v16 offset:3072
	ds_read_b32 v9, v17 offset:3072
	ds_read_b32 v12, v16 offset:4096
	ds_read_b32 v14, v17 offset:4096
	ds_read_b32 v13, v16 offset:5120
	ds_read_b32 v15, v17 offset:5120
	s_waitcnt lgkmcnt(0)
	v_pk_add_f32 v[0:1], v[0:1], v[2:3]
	v_mov_b32_e32 v2, s70
	v_mov_b32_e32 v3, s71
	v_mov_b64_e32 v[10:11], s[68:69]
	v_pk_add_f32 v[6:7], v[6:7], v[8:9]
	v_pk_fma_f32 v[0:1], v[0:1], s[4:5], v[10:11] op_sel_hi:[1,0,1]
	v_pk_fma_f32 v[2:3], v[6:7], s[4:5], v[2:3] op_sel_hi:[1,0,1]
	global_store_dwordx4 v[4:5], v[0:3], off
	s_nop 1
	v_pk_add_f32 v[0:1], v[12:13], v[14:15]
	v_mov_b64_e32 v[2:3], s[72:73]
	v_pk_fma_f32 v[0:1], v[0:1], s[4:5], v[2:3] op_sel_hi:[1,0,1]
	global_store_dwordx2 v[4:5], v[0:1], off offset:16
	s_endpgm
